# pj K-loop: trailing s_barrier of each MFMA section moved up 16 MFMAs (partner starts while 16 MFMAs remain)
# baseline (speedup 1.0000x reference)
; #define PG8_STAGE(bufoff, gbase, voff) do { _Pragma("unroll") for (int _i = 0; _i < 2; ++_i) \
;         __builtin_amdgcn_global_load_lds((const unsigned*)((const char*)(gbase) + (voff)[_i]), (LAS unsigned*)(lds + (bufoff) + ldsw + _i * 8192), 16, 0, 0); } while (0)
; #define PG8_LDA(dst, b, h) do { _Pragma("unroll") for (int m = 0; m < 4; ++m) _Pragma("unroll") for (int k = 0; k < 2; ++k) dst[m][k] = *(const LAS bf16x8*)(lds + PG8_SA(b, h) + aoff + m * 2048 + k * 1024); } while (0)
; #define PG8_LDB(dst, b, h) do { _Pragma("unroll") for (int n = 0; n < 2; ++n) _Pragma("unroll") for (int k = 0; k < 2; ++k) dst[n][k] = *(const LAS bf16x8*)(lds + PG8_SB(b, h) + boff + n * 2048 + k * 1024); } while (0)
; #define PG8_MMA(ai, bj, At, Bt) do { __builtin_amdgcn_s_setprio(1); _Pragma("unroll") for (int m = 0; m < 4; ++m) _Pragma("unroll") for (int n = 0; n < 2; ++n) _Pragma("unroll") for (int k = 0; k < 2; ++k) \
;         acc[ai][bj][m][n] = __builtin_amdgcn_mfma_f32_16x16x32_bf16(Bt[n][k], At[m][k], acc[ai][bj][m][n], 0, 0, 0); __builtin_amdgcn_s_setprio(0); } while (0)
; #define PG8_WAIT_V(n) asm volatile("s_waitcnt vmcnt(" #n ")" ::: "memory")
; #define PG8_WAIT_L(n) asm volatile("s_waitcnt lgkmcnt(" #n ")" ::: "memory")
; #define PG8_BAR __builtin_amdgcn_s_barrier()
; #define PG8_SCHED __builtin_amdgcn_sched_barrier(0)
; #define PG8_STAGE(bufoff, gbase, voff) do { _Pragma("unroll") for (int _i = 0; _i < 2; ++_i) \
;         __builtin_amdgcn_global_load_lds((const unsigned*)((const char*)(gbase) + (voff)[_i]), (LAS unsigned*)(lds + (bufoff) + ldsw + _i * 8192), 16, 0, 0); } while (0)
; #define PG8_LDA(dst, b, h) do { _Pragma("unroll") for (int m = 0; m < 4; ++m) _Pragma("unroll") for (int k = 0; k < 2; ++k) dst[m][k] = *(const LAS bf16x8*)(lds + PG8_SA(b, h) + aoff + m * 2048 + k * 1024); } while (0)
;     ...
;             PG8_LDB(B0, 0, 0); PG8_LDB(B1, 0, 1); PG8_SCHED; PG8_LDA(At, 0, 0); PG8_STAGE(PG8_SA(1, 1), a1 + hstepA, voffA);
;             PG8_WAIT_V(8); PG8_WAIT_L(0); PG8_BAR; PG8_MMA(0, 0, At, B0); PG8_MMA(0, 1, At, B1); PG8_BAR; PG8_SCHED;
;             PG8_LDA(At, 0, 1); PG8_STAGE(PG8_SB(0, 0), b2, voffB); PG8_STAGE(PG8_SB(0, 1), b2 + hstep, voffB); PG8_STAGE(PG8_SA(0, 0), a2, voffA);
;             PG8_WAIT_V(8); PG8_WAIT_L(0); PG8_BAR; if (hi_on) { PG8_MMA(1, 0, At, B0); PG8_MMA(1, 1, At, B1); } PG8_BAR; PG8_SCHED;
.LBB0_213:
	s_add_u32 s22, s6, 0xfffc0080
	s_addc_u32 s23, s7, -1
	s_add_i32 s27, 0, 0x10000
	s_cmp_eq_u32 s26, 12
	s_cselect_b32 s25, s19, s23
	s_cselect_b32 s24, s18, s22
	v_add_u32_e32 v52, s27, v1
	s_cselect_b32 s23, s21, s17
	s_cselect_b32 s22, s20, s15
	s_add_i32 s42, 0, 0x14000
	ds_read_b128 v[62:65], v52
	ds_read_b128 v[66:69], v52 offset:1024
	ds_read_b128 v[156:159], v52 offset:2048
	ds_read_b128 v[160:163], v52 offset:3072
	v_add_u32_e32 v52, s42, v1
	ds_read_b128 v[168:171], v52
	ds_read_b128 v[172:175], v52 offset:1024
	ds_read_b128 v[176:179], v52 offset:2048
	ds_read_b128 v[180:183], v52 offset:3072
	v_lshl_add_u64 v[52:53], s[6:7], 0, v[152:153]
	s_add_i32 m0, s30, 0xc000
	ds_read_b128 v[184:187], v166
	ds_read_b128 v[188:191], v166 offset:1024
	ds_read_b128 v[192:195], v166 offset:2048
	ds_read_b128 v[204:207], v166 offset:3072
	ds_read_b128 v[208:211], v166 offset:4096
	ds_read_b128 v[212:215], v166 offset:5120
	ds_read_b128 v[216:219], v166 offset:6144
	ds_read_b128 v[220:223], v166 offset:7168
	global_load_lds_dwordx4 v[52:53], off
	v_lshl_add_u64 v[52:53], s[6:7], 0, v[154:155]
	s_add_i32 m0, s30, 0xe000
	s_nop 0
	global_load_lds_dwordx4 v[52:53], off
	s_waitcnt vmcnt(8)
	s_waitcnt lgkmcnt(0)
	s_barrier
	s_setprio 1
	s_waitcnt lgkmcnt(0)
	v_mfma_f32_16x16x32_bf16 v[138:141], v[62:65], v[184:187], v[138:141]
	v_mfma_f32_16x16x32_bf16 v[134:137], v[156:159], v[184:187], v[134:137]
	v_mfma_f32_16x16x32_bf16 v[122:125], v[62:65], v[192:195], v[122:125]
	v_mfma_f32_16x16x32_bf16 v[118:121], v[156:159], v[192:195], v[118:121]
	v_mfma_f32_16x16x32_bf16 v[106:109], v[62:65], v[208:211], v[106:109]
	v_mfma_f32_16x16x32_bf16 v[102:105], v[156:159], v[208:211], v[102:105]
	v_mfma_f32_16x16x32_bf16 v[90:93], v[62:65], v[216:219], v[90:93]
	v_mfma_f32_16x16x32_bf16 v[86:89], v[156:159], v[216:219], v[86:89]
	v_mfma_f32_16x16x32_bf16 v[138:141], v[66:69], v[188:191], v[138:141]
	v_mfma_f32_16x16x32_bf16 v[134:137], v[160:163], v[188:191], v[134:137]
	v_mfma_f32_16x16x32_bf16 v[122:125], v[66:69], v[204:207], v[122:125]
	v_mfma_f32_16x16x32_bf16 v[118:121], v[160:163], v[204:207], v[118:121]
	v_mfma_f32_16x16x32_bf16 v[106:109], v[66:69], v[212:215], v[106:109]
	v_mfma_f32_16x16x32_bf16 v[102:105], v[160:163], v[212:215], v[102:105]
	v_mfma_f32_16x16x32_bf16 v[90:93], v[66:69], v[220:223], v[90:93]
	v_mfma_f32_16x16x32_bf16 v[86:89], v[160:163], v[220:223], v[86:89]
	s_setprio 0
	s_setprio 1
	s_barrier
	v_mfma_f32_16x16x32_bf16 v[130:133], v[168:171], v[184:187], v[130:133]
	v_mfma_f32_16x16x32_bf16 v[126:129], v[176:179], v[184:187], v[126:129]
	v_mfma_f32_16x16x32_bf16 v[114:117], v[168:171], v[192:195], v[114:117]
	v_mfma_f32_16x16x32_bf16 v[110:113], v[176:179], v[192:195], v[110:113]
	v_mfma_f32_16x16x32_bf16 v[98:101], v[168:171], v[208:211], v[98:101]
	v_mfma_f32_16x16x32_bf16 v[94:97], v[176:179], v[208:211], v[94:97]
	v_mfma_f32_16x16x32_bf16 v[82:85], v[168:171], v[216:219], v[82:85]
	v_mfma_f32_16x16x32_bf16 v[78:81], v[176:179], v[216:219], v[78:81]
	v_mfma_f32_16x16x32_bf16 v[130:133], v[172:175], v[188:191], v[130:133]
	v_mfma_f32_16x16x32_bf16 v[126:129], v[180:183], v[188:191], v[126:129]
	v_mfma_f32_16x16x32_bf16 v[114:117], v[172:175], v[204:207], v[114:117]
	v_mfma_f32_16x16x32_bf16 v[110:113], v[180:183], v[204:207], v[110:113]
	v_mfma_f32_16x16x32_bf16 v[98:101], v[172:175], v[212:215], v[98:101]
	v_mfma_f32_16x16x32_bf16 v[94:97], v[180:183], v[212:215], v[94:97]
	v_mfma_f32_16x16x32_bf16 v[82:85], v[172:175], v[220:223], v[82:85]
	v_mfma_f32_16x16x32_bf16 v[78:81], v[180:183], v[220:223], v[78:81]
	s_setprio 0
	s_add_i32 s27, s27, s29
	v_lshl_add_u64 v[196:197], s[22:23], 0, v[144:145]
	s_mov_b32 m0, s27
	ds_read_b128 v[184:187], v166 offset:16384
	ds_read_b128 v[188:191], v166 offset:17408
	ds_read_b128 v[192:195], v166 offset:18432
	ds_read_b128 v[204:207], v166 offset:19456
	ds_read_b128 v[208:211], v166 offset:20480
	ds_read_b128 v[212:215], v166 offset:21504
	ds_read_b128 v[216:219], v166 offset:22528
	ds_read_b128 v[220:223], v166 offset:23552
	global_load_lds_dwordx4 v[196:197], off
	s_add_i32 m0, s27, 0x2000
	s_add_u32 s36, s22, 0x40000
	v_lshl_add_u64 v[224:225], s[22:23], 0, v[148:149]
	s_addc_u32 s37, s23, 0
	s_add_i32 s27, s42, s29
	global_load_lds_dwordx4 v[224:225], off
	v_lshl_add_u64 v[52:53], s[36:37], 0, v[144:145]
	s_mov_b32 m0, s27
	v_lshl_add_u64 v[226:227], s[24:25], 0, v[142:143]
	global_load_lds_dwordx4 v[52:53], off
	v_lshl_add_u64 v[52:53], s[36:37], 0, v[148:149]
	s_add_i32 m0, s27, 0x2000
	v_lshl_add_u64 v[228:229], s[24:25], 0, v[146:147]
	global_load_lds_dwordx4 v[52:53], off
	s_mov_b32 m0, s30
	s_nop 0
	global_load_lds_dwordx4 v[226:227], off
	s_mov_b32 m0, s31
	s_nop 0
	global_load_lds_dwordx4 v[228:229], off
	s_waitcnt vmcnt(8)
	s_waitcnt lgkmcnt(0)
	s_barrier
	s_setprio 1
	s_waitcnt lgkmcnt(0)
	v_mfma_f32_16x16x32_bf16 v[74:77], v[62:65], v[184:187], v[74:77]
	v_mfma_f32_16x16x32_bf16 v[70:73], v[156:159], v[184:187], v[70:73]
	v_mfma_f32_16x16x32_bf16 v[48:51], v[62:65], v[192:195], v[48:51]
	v_mfma_f32_16x16x32_bf16 v[44:47], v[156:159], v[192:195], v[44:47]
	v_mfma_f32_16x16x32_bf16 v[30:33], v[62:65], v[208:211], v[30:33]
	v_mfma_f32_16x16x32_bf16 v[26:29], v[156:159], v[208:211], v[26:29]
	v_mfma_f32_16x16x32_bf16 v[14:17], v[62:65], v[216:219], v[14:17]
	v_mfma_f32_16x16x32_bf16 v[10:13], v[156:159], v[216:219], v[10:13]
	v_mfma_f32_16x16x32_bf16 v[74:77], v[66:69], v[188:191], v[74:77]
	v_mfma_f32_16x16x32_bf16 v[70:73], v[160:163], v[188:191], v[70:73]
	v_mfma_f32_16x16x32_bf16 v[48:51], v[66:69], v[204:207], v[48:51]
	v_mfma_f32_16x16x32_bf16 v[44:47], v[160:163], v[204:207], v[44:47]
	v_mfma_f32_16x16x32_bf16 v[30:33], v[66:69], v[212:215], v[30:33]
	v_mfma_f32_16x16x32_bf16 v[26:29], v[160:163], v[212:215], v[26:29]
	v_mfma_f32_16x16x32_bf16 v[14:17], v[66:69], v[220:223], v[14:17]
	v_mfma_f32_16x16x32_bf16 v[10:13], v[160:163], v[220:223], v[10:13]
	s_setprio 0
	s_setprio 1
	s_barrier
; #define PG8_STAGE(bufoff, gbase, voff) do { _Pragma("unroll") for (int _i = 0; _i < 2; ++_i) \
;         __builtin_amdgcn_global_load_lds((const unsigned*)((const char*)(gbase) + (voff)[_i]), (LAS unsigned*)(lds + (bufoff) + ldsw + _i * 8192), 16, 0, 0); } while (0)
; #define PG8_LDA(dst, b, h) do { _Pragma("unroll") for (int m = 0; m < 4; ++m) _Pragma("unroll") for (int k = 0; k < 2; ++k) dst[m][k] = *(const LAS bf16x8*)(lds + PG8_SA(b, h) + aoff + m * 2048 + k * 1024); } while (0)
; #define PG8_LDB(dst, b, h) do { _Pragma("unroll") for (int n = 0; n < 2; ++n) _Pragma("unroll") for (int k = 0; k < 2; ++k) dst[n][k] = *(const LAS bf16x8*)(lds + PG8_SB(b, h) + boff + n * 2048 + k * 1024); } while (0)
; #define PG8_MMA(ai, bj, At, Bt) do { __builtin_amdgcn_s_setprio(1); _Pragma("unroll") for (int m = 0; m < 4; ++m) _Pragma("unroll") for (int n = 0; n < 2; ++n) _Pragma("unroll") for (int k = 0; k < 2; ++k) \
;         acc[ai][bj][m][n] = __builtin_amdgcn_mfma_f32_16x16x32_bf16(Bt[n][k], At[m][k], acc[ai][bj][m][n], 0, 0, 0); __builtin_amdgcn_s_setprio(0); } while (0)
; #define PG8_WAIT_V(n) asm volatile("s_waitcnt vmcnt(" #n ")" ::: "memory")
; #define PG8_WAIT_L(n) asm volatile("s_waitcnt lgkmcnt(" #n ")" ::: "memory")
; #define PG8_BAR __builtin_amdgcn_s_barrier()
; #define PG8_SCHED __builtin_amdgcn_sched_barrier(0)
; #define PG8_STAGE(bufoff, gbase, voff) do { _Pragma("unroll") for (int _i = 0; _i < 2; ++_i) \
;         __builtin_amdgcn_global_load_lds((const unsigned*)((const char*)(gbase) + (voff)[_i]), (LAS unsigned*)(lds + (bufoff) + ldsw + _i * 8192), 16, 0, 0); } while (0)
; #define PG8_LDA(dst, b, h) do { _Pragma("unroll") for (int m = 0; m < 4; ++m) _Pragma("unroll") for (int k = 0; k < 2; ++k) dst[m][k] = *(const LAS bf16x8*)(lds + PG8_SA(b, h) + aoff + m * 2048 + k * 1024); } while (0)
; #define PG8_WAIT_V(n) asm volatile("s_waitcnt vmcnt(" #n ")" ::: "memory")
; #define PG8_WAIT_L(n) asm volatile("s_waitcnt lgkmcnt(" #n ")" ::: "memory")
;     ...
;             PG8_WAIT_V(8); PG8_WAIT_L(0); PG8_BAR; if (hi_on) { PG8_MMA(1, 0, At, B0); PG8_MMA(1, 1, At, B1); } PG8_BAR; PG8_SCHED;
;             PG8_LDB(B0, 1, 0); PG8_LDB(B1, 1, 1); PG8_SCHED; PG8_LDA(At, 1, 0); PG8_STAGE(PG8_SA(0, 1), a2 + hstepA, voffA);
;             PG8_WAIT_V(8); PG8_WAIT_L(0); PG8_BAR; PG8_MMA(0, 0, At, B0); PG8_MMA(0, 1, At, B1); PG8_BAR; PG8_SCHED;
	v_mfma_f32_16x16x32_bf16 v[58:61], v[168:171], v[184:187], v[58:61]
	v_mfma_f32_16x16x32_bf16 v[52:55], v[176:179], v[184:187], v[54:57]
	v_mfma_f32_16x16x32_bf16 v[40:43], v[168:171], v[192:195], v[40:43]
	v_mfma_f32_16x16x32_bf16 v[36:39], v[176:179], v[192:195], v[36:39]
	v_mfma_f32_16x16x32_bf16 v[22:25], v[168:171], v[208:211], v[22:25]
	v_mfma_f32_16x16x32_bf16 v[18:21], v[176:179], v[208:211], v[18:21]
	v_mfma_f32_16x16x32_bf16 v[6:9], v[168:171], v[216:219], v[6:9]
	v_mfma_f32_16x16x32_bf16 v[2:5], v[176:179], v[216:219], v[2:5]
	v_mfma_f32_16x16x32_bf16 v[58:61], v[172:175], v[188:191], v[58:61]
	v_mfma_f32_16x16x32_bf16 v[52:55], v[180:183], v[188:191], v[52:55]
	v_mfma_f32_16x16x32_bf16 v[40:43], v[172:175], v[204:207], v[40:43]
	v_mfma_f32_16x16x32_bf16 v[36:39], v[180:183], v[204:207], v[36:39]
	v_mfma_f32_16x16x32_bf16 v[22:25], v[172:175], v[212:215], v[22:25]
	v_mfma_f32_16x16x32_bf16 v[18:21], v[180:183], v[212:215], v[18:21]
	v_mfma_f32_16x16x32_bf16 v[6:9], v[172:175], v[220:223], v[6:9]
	v_mfma_f32_16x16x32_bf16 v[2:5], v[180:183], v[220:223], v[2:5]
	s_setprio 0
	s_add_i32 s27, 0, 0x18000
	v_add_u32_e32 v56, s27, v1
	s_add_i32 s36, 0, 0x1c000
	ds_read_b128 v[62:65], v56
	ds_read_b128 v[66:69], v56 offset:1024
	ds_read_b128 v[156:159], v56 offset:2048
	ds_read_b128 v[160:163], v56 offset:3072
	v_add_u32_e32 v56, s36, v1
	ds_read_b128 v[168:171], v56
	ds_read_b128 v[172:175], v56 offset:1024
	ds_read_b128 v[176:179], v56 offset:2048
	ds_read_b128 v[180:183], v56 offset:3072
	s_add_u32 s24, s24, 0x40000
	s_addc_u32 s25, s25, 0
	s_mov_b32 m0, s34
	v_lshl_add_u64 v[56:57], s[24:25], 0, v[142:143]
	ds_read_b128 v[184:187], v166 offset:32768
	ds_read_b128 v[188:191], v166 offset:33792
	ds_read_b128 v[192:195], v166 offset:34816
	ds_read_b128 v[204:207], v166 offset:35840
	ds_read_b128 v[208:211], v166 offset:36864
	ds_read_b128 v[212:215], v166 offset:37888
	ds_read_b128 v[216:219], v166 offset:38912
	ds_read_b128 v[220:223], v166 offset:39936
	global_load_lds_dwordx4 v[56:57], off
	v_lshl_add_u64 v[56:57], s[24:25], 0, v[146:147]
	s_mov_b32 m0, s35
	s_nop 0
	global_load_lds_dwordx4 v[56:57], off
	s_waitcnt vmcnt(8)
	s_waitcnt lgkmcnt(0)
	s_barrier
	s_setprio 1
	s_waitcnt lgkmcnt(0)
	v_mfma_f32_16x16x32_bf16 v[138:141], v[62:65], v[184:187], v[138:141]
	v_mfma_f32_16x16x32_bf16 v[134:137], v[156:159], v[184:187], v[134:137]
	v_mfma_f32_16x16x32_bf16 v[122:125], v[62:65], v[192:195], v[122:125]
	v_mfma_f32_16x16x32_bf16 v[118:121], v[156:159], v[192:195], v[118:121]
	v_mfma_f32_16x16x32_bf16 v[106:109], v[62:65], v[208:211], v[106:109]
	v_mfma_f32_16x16x32_bf16 v[102:105], v[156:159], v[208:211], v[102:105]
	v_mfma_f32_16x16x32_bf16 v[90:93], v[62:65], v[216:219], v[90:93]
	v_mfma_f32_16x16x32_bf16 v[86:89], v[156:159], v[216:219], v[86:89]
	v_mfma_f32_16x16x32_bf16 v[138:141], v[66:69], v[188:191], v[138:141]
	v_mfma_f32_16x16x32_bf16 v[134:137], v[160:163], v[188:191], v[134:137]
	v_mfma_f32_16x16x32_bf16 v[122:125], v[66:69], v[204:207], v[122:125]
	v_mfma_f32_16x16x32_bf16 v[118:121], v[160:163], v[204:207], v[118:121]
	v_mfma_f32_16x16x32_bf16 v[106:109], v[66:69], v[212:215], v[106:109]
	v_mfma_f32_16x16x32_bf16 v[102:105], v[160:163], v[212:215], v[102:105]
	v_mfma_f32_16x16x32_bf16 v[90:93], v[66:69], v[220:223], v[90:93]
	v_mfma_f32_16x16x32_bf16 v[86:89], v[160:163], v[220:223], v[86:89]
	s_setprio 0
	s_setprio 1
	s_barrier
; #define PG8_STAGE(bufoff, gbase, voff) do { _Pragma("unroll") for (int _i = 0; _i < 2; ++_i) \
;         __builtin_amdgcn_global_load_lds((const unsigned*)((const char*)(gbase) + (voff)[_i]), (LAS unsigned*)(lds + (bufoff) + ldsw + _i * 8192), 16, 0, 0); } while (0)
; #define PG8_LDA(dst, b, h) do { _Pragma("unroll") for (int m = 0; m < 4; ++m) _Pragma("unroll") for (int k = 0; k < 2; ++k) dst[m][k] = *(const LAS bf16x8*)(lds + PG8_SA(b, h) + aoff + m * 2048 + k * 1024); } while (0)
; #define PG8_MMA(ai, bj, At, Bt) do { __builtin_amdgcn_s_setprio(1); _Pragma("unroll") for (int m = 0; m < 4; ++m) _Pragma("unroll") for (int n = 0; n < 2; ++n) _Pragma("unroll") for (int k = 0; k < 2; ++k) \
;         acc[ai][bj][m][n] = __builtin_amdgcn_mfma_f32_16x16x32_bf16(Bt[n][k], At[m][k], acc[ai][bj][m][n], 0, 0, 0); __builtin_amdgcn_s_setprio(0); } while (0)
; #define PG8_WAIT_V(n) asm volatile("s_waitcnt vmcnt(" #n ")" ::: "memory")
; #define PG8_WAIT_L(n) asm volatile("s_waitcnt lgkmcnt(" #n ")" ::: "memory")
; #define PG8_BAR __builtin_amdgcn_s_barrier()
; #define PG8_SCHED __builtin_amdgcn_sched_barrier(0)
; #define PG8_STAGE(bufoff, gbase, voff) do { _Pragma("unroll") for (int _i = 0; _i < 2; ++_i) \
;         __builtin_amdgcn_global_load_lds((const unsigned*)((const char*)(gbase) + (voff)[_i]), (LAS unsigned*)(lds + (bufoff) + ldsw + _i * 8192), 16, 0, 0); } while (0)
; #define PG8_LDA(dst, b, h) do { _Pragma("unroll") for (int m = 0; m < 4; ++m) _Pragma("unroll") for (int k = 0; k < 2; ++k) dst[m][k] = *(const LAS bf16x8*)(lds + PG8_SA(b, h) + aoff + m * 2048 + k * 1024); } while (0)
; #define PG8_MMA(ai, bj, At, Bt) do { __builtin_amdgcn_s_setprio(1); _Pragma("unroll") for (int m = 0; m < 4; ++m) _Pragma("unroll") for (int n = 0; n < 2; ++n) _Pragma("unroll") for (int k = 0; k < 2; ++k) \
;         acc[ai][bj][m][n] = __builtin_amdgcn_mfma_f32_16x16x32_bf16(Bt[n][k], At[m][k], acc[ai][bj][m][n], 0, 0, 0); __builtin_amdgcn_s_setprio(0); } while (0)
;     ...
;             PG8_WAIT_V(8); PG8_WAIT_L(0); PG8_BAR; PG8_MMA(0, 0, At, B0); PG8_MMA(0, 1, At, B1); PG8_BAR; PG8_SCHED;
;             PG8_LDA(At, 1, 1); PG8_STAGE(PG8_SB(1, 0), b3, voffB); PG8_STAGE(PG8_SB(1, 1), b3 + hstep, voffB); PG8_STAGE(PG8_SA(1, 0), a3, voffA);
;             PG8_WAIT_V(8); PG8_WAIT_L(0); PG8_BAR; if (hi_on) { PG8_MMA(1, 0, At, B0); PG8_MMA(1, 1, At, B1); } PG8_BAR; PG8_SCHED;
;         }
	v_mfma_f32_16x16x32_bf16 v[130:133], v[168:171], v[184:187], v[130:133]
	v_mfma_f32_16x16x32_bf16 v[126:129], v[176:179], v[184:187], v[126:129]
	v_mfma_f32_16x16x32_bf16 v[114:117], v[168:171], v[192:195], v[114:117]
	v_mfma_f32_16x16x32_bf16 v[110:113], v[176:179], v[192:195], v[110:113]
	v_mfma_f32_16x16x32_bf16 v[98:101], v[168:171], v[208:211], v[98:101]
	v_mfma_f32_16x16x32_bf16 v[94:97], v[176:179], v[208:211], v[94:97]
	v_mfma_f32_16x16x32_bf16 v[82:85], v[168:171], v[216:219], v[82:85]
	v_mfma_f32_16x16x32_bf16 v[78:81], v[176:179], v[216:219], v[78:81]
	v_mfma_f32_16x16x32_bf16 v[130:133], v[172:175], v[188:191], v[130:133]
	v_mfma_f32_16x16x32_bf16 v[126:129], v[180:183], v[188:191], v[126:129]
	v_mfma_f32_16x16x32_bf16 v[114:117], v[172:175], v[204:207], v[114:117]
	v_mfma_f32_16x16x32_bf16 v[110:113], v[180:183], v[204:207], v[110:113]
	v_mfma_f32_16x16x32_bf16 v[98:101], v[172:175], v[212:215], v[98:101]
	v_mfma_f32_16x16x32_bf16 v[94:97], v[180:183], v[212:215], v[94:97]
	v_mfma_f32_16x16x32_bf16 v[82:85], v[172:175], v[220:223], v[82:85]
	v_mfma_f32_16x16x32_bf16 v[78:81], v[180:183], v[220:223], v[78:81]
	s_setprio 0
	s_add_i32 s24, s27, s29
	v_lshl_add_u64 v[56:57], v[196:197], 0, s[88:89]
	s_mov_b32 m0, s24
	ds_read_b128 v[184:187], v166 offset:49152
	ds_read_b128 v[188:191], v166 offset:50176
	ds_read_b128 v[192:195], v166 offset:51200
	ds_read_b128 v[204:207], v166 offset:52224
	ds_read_b128 v[208:211], v166 offset:53248
	ds_read_b128 v[212:215], v166 offset:54272
	ds_read_b128 v[216:219], v166 offset:55296
	ds_read_b128 v[220:223], v166 offset:56320
	global_load_lds_dwordx4 v[56:57], off
	s_add_i32 m0, s24, 0x2000
	s_add_u32 s22, s22, 0x40080
	v_lshl_add_u64 v[56:57], v[224:225], 0, s[88:89]
	s_addc_u32 s23, s23, 0
	s_add_i32 s24, s36, s29
	global_load_lds_dwordx4 v[56:57], off
	v_lshl_add_u64 v[56:57], s[22:23], 0, v[144:145]
	s_mov_b32 m0, s24
	s_nop 0
	global_load_lds_dwordx4 v[56:57], off
	v_lshl_add_u64 v[56:57], s[22:23], 0, v[148:149]
	s_add_i32 m0, s24, 0x2000
	s_nop 0
	global_load_lds_dwordx4 v[56:57], off
	v_lshl_add_u64 v[56:57], v[226:227], 0, s[88:89]
	s_mov_b32 m0, s39
	s_nop 0
	global_load_lds_dwordx4 v[56:57], off
	v_lshl_add_u64 v[56:57], v[228:229], 0, s[88:89]
	s_mov_b32 m0, s40
	s_nop 0
	global_load_lds_dwordx4 v[56:57], off
	s_waitcnt vmcnt(8)
	s_waitcnt lgkmcnt(0)
	s_barrier
	s_setprio 1
	s_waitcnt lgkmcnt(0)
	v_mfma_f32_16x16x32_bf16 v[74:77], v[62:65], v[184:187], v[74:77]
	v_mfma_f32_16x16x32_bf16 v[70:73], v[156:159], v[184:187], v[70:73]
	v_mfma_f32_16x16x32_bf16 v[48:51], v[62:65], v[192:195], v[48:51]
	v_mfma_f32_16x16x32_bf16 v[44:47], v[156:159], v[192:195], v[44:47]
	v_mfma_f32_16x16x32_bf16 v[30:33], v[62:65], v[208:211], v[30:33]
	v_mfma_f32_16x16x32_bf16 v[26:29], v[156:159], v[208:211], v[26:29]
	v_mfma_f32_16x16x32_bf16 v[14:17], v[62:65], v[216:219], v[14:17]
	v_mfma_f32_16x16x32_bf16 v[10:13], v[156:159], v[216:219], v[10:13]
	v_mfma_f32_16x16x32_bf16 v[74:77], v[66:69], v[188:191], v[74:77]
	v_mfma_f32_16x16x32_bf16 v[70:73], v[160:163], v[188:191], v[70:73]
	v_mfma_f32_16x16x32_bf16 v[48:51], v[66:69], v[204:207], v[48:51]
	v_mfma_f32_16x16x32_bf16 v[44:47], v[160:163], v[204:207], v[44:47]
	v_mfma_f32_16x16x32_bf16 v[30:33], v[66:69], v[212:215], v[30:33]
	v_mfma_f32_16x16x32_bf16 v[26:29], v[160:163], v[212:215], v[26:29]
	v_mfma_f32_16x16x32_bf16 v[14:17], v[66:69], v[220:223], v[14:17]
	v_mfma_f32_16x16x32_bf16 v[10:13], v[160:163], v[220:223], v[10:13]
	s_setprio 0
	s_setprio 1
	s_barrier
	v_mfma_f32_16x16x32_bf16 v[56:59], v[168:171], v[184:187], v[58:61]
	v_mfma_f32_16x16x32_bf16 v[52:55], v[176:179], v[184:187], v[52:55]
	v_mfma_f32_16x16x32_bf16 v[40:43], v[168:171], v[192:195], v[40:43]
	v_mfma_f32_16x16x32_bf16 v[36:39], v[176:179], v[192:195], v[36:39]
	v_mfma_f32_16x16x32_bf16 v[22:25], v[168:171], v[208:211], v[22:25]
	v_mfma_f32_16x16x32_bf16 v[18:21], v[176:179], v[208:211], v[18:21]
	v_mfma_f32_16x16x32_bf16 v[6:9], v[168:171], v[216:219], v[6:9]
	v_mfma_f32_16x16x32_bf16 v[2:5], v[176:179], v[216:219], v[2:5]
	v_mfma_f32_16x16x32_bf16 v[58:61], v[172:175], v[188:191], v[56:59]
	v_mfma_f32_16x16x32_bf16 v[54:57], v[180:183], v[188:191], v[52:55]
	v_mfma_f32_16x16x32_bf16 v[40:43], v[172:175], v[204:207], v[40:43]
	v_mfma_f32_16x16x32_bf16 v[36:39], v[180:183], v[204:207], v[36:39]
	v_mfma_f32_16x16x32_bf16 v[22:25], v[172:175], v[212:215], v[22:25]
	v_mfma_f32_16x16x32_bf16 v[18:21], v[180:183], v[212:215], v[18:21]
	v_mfma_f32_16x16x32_bf16 v[6:9], v[172:175], v[220:223], v[6:9]
	v_mfma_f32_16x16x32_bf16 v[2:5], v[180:183], v[220:223], v[2:5]
	s_setprio 0
	s_add_i32 s26, s26, 2
	s_add_u32 s6, s6, 0x100
	s_addc_u32 s7, s7, 0
	s_add_u32 s15, s15, 0x100
	s_addc_u32 s17, s17, 0
	s_cmp_gt_u32 s26, 13
	s_cbranch_scc0 .LBB0_213
	s_and_b64 vcc, exec, s[12:13]
	s_cbranch_vccz .LBB0_216
	s_barrier
